# c3: v^T staging with DPP pair exchange + dword LDS writes (layout unchanged) on top of split/p8conv/lean/ln1fill/ln1sc1/earlyinv
# baseline (speedup 1.0000x reference)
.LBB0_658:
	v_writelane_b32 v247, s23, 38
	s_andn2_b64 vcc, exec, s[8:9]
	v_writelane_b32 v247, s91, 39
	s_cbranch_vccnz .LBB0_709
	v_readlane_b32 s0, v247, 36
	v_readlane_b32 s1, v247, 37
	s_lshl_b32 s66, s0, 7
	s_lshl_b64 s[0:1], s[66:67], 2
	s_add_u32 s0, s12, s0
	s_addc_u32 s1, s11, s1
	s_lshl_b32 s5, s4, 4
	s_cmp_gt_u32 s49, 1
	v_lshlrev_b32_e32 v36, 4, v35
	s_cselect_b64 s[94:95], -1, 0
	v_ashrrev_i32_e32 v104, 3, v35
	v_and_b32_e32 v36, 0x70, v36
	s_movk_i32 s11, 0x90
	s_and_b64 s[2:3], s[94:95], exec
	v_mad_u64_u32 v[90:91], s[2:3], v104, s11, v[36:37]
	s_cselect_b32 s64, 6, 0
	s_lshl_b32 s8, s4, 5
	v_lshlrev_b32_e32 v40, 3, v35
	s_ashr_i32 s2, s5, 31
	s_add_i32 s9, s8, 0
	v_lshl_add_u32 v37, v104, 1, 0
	v_and_b32_e32 v92, 0x78, v40
	v_and_b32_e32 v43, 15, v35
	v_mov_b32_e32 v41, s2
	s_ashr_i32 s2, s10, 3
	s_add_i32 s9, s9, 0x14800
	v_mul_u32_u24_e32 v39, 0x90, v36
	v_mad_u32_u24 v91, v36, s11, v37
	v_mov_b32_e32 v36, s5
	v_or_b32_e32 v40, s5, v43
	s_ashr_i32 s5, s4, 31
	s_and_b32 s3, s2, -16
	v_lshl_add_u32 v53, v43, 1, s9
	s_lshl_b32 s9, s4, 8
	s_add_i32 s35, 0, 0x14000
	v_lshlrev_b32_e32 v68, 2, v92
	s_lshl_b32 s34, s49, 6
	s_lshl_b32 s96, s49, 7
	v_bfi_b32 v42, -16, s2, v35
	s_add_i32 s2, s3, 64
	s_add_i32 s51, s35, s9
	v_lshl_add_u64 v[94:95], s[0:1], 0, v[68:69]
	s_lshl_b64 s[0:1], s[4:5], 10
	s_add_u32 s0, s38, s0
	v_lshlrev_b32_e32 v68, 4, v67
	s_addc_u32 s1, s39, s1
	s_movk_i32 s36, 0x48
	v_lshl_add_u64 v[44:45], s[0:1], 0, v[68:69]
	s_mov_b64 s[0:1], 0x5f17a100
	v_mul_f32_e32 v34, 0x4f7ffffe, v34
	v_lshrrev_b32_e32 v46, 4, v67
	v_mul_lo_u32 v47, v42, s36
	v_or_b32_e32 v42, s2, v43
	v_lshl_add_u64 v[96:97], v[44:45], 0, s[0:1]
	v_and_or_b32 v44, s8, 32, v43
	v_cvt_u32_f32_e32 v34, v34
	v_and_b32_e32 v38, 7, v35
	v_ashrrev_i32_e32 v106, 4, v35
	v_mul_lo_u32 v49, v42, s36
	v_lshl_or_b32 v51, v46, 2, s3
	v_and_b32_e32 v42, 48, v35
	v_mul_lo_u32 v35, v40, s11
	v_lshlrev_b64 v[40:41], 7, v[40:41]
	v_or_b32_e32 v79, 16, v44
	v_lshlrev_b32_e32 v48, 3, v46
	v_lshl_add_u64 v[40:41], s[6:7], 0, v[40:41]
	v_cmp_gt_i32_e64 s[4:5], v44, v51
	v_cmp_lt_i32_e64 s[6:7], v44, v51
	v_mul_lo_u32 v56, v51, s11
	v_or_b32_e32 v57, 1, v51
	v_or_b32_e32 v68, 2, v51
	v_or_b32_e32 v78, 3, v51
	v_cmp_gt_i32_e64 s[18:19], v79, v51
	v_cmp_lt_i32_e64 s[20:21], v79, v51
	v_lshlrev_b32_e32 v51, 1, v79
	v_mad_u32_u24 v105, v67, s11, v36
	v_or_b32_e32 v50, 0x1200, v48
	v_cmp_eq_u32_e64 s[2:3], 0, v43
	v_mul_u32_u24_e32 v45, 0x48, v44
	v_lshl_add_u32 v55, v44, 1, s92
	v_cmp_gt_i32_e64 s[8:9], v44, v57
	v_cmp_gt_i32_e64 s[10:11], v44, v68
	v_cmp_lt_i32_e64 s[12:13], v44, v68
	v_cmp_gt_i32_e64 s[14:15], v44, v78
	v_cmp_lt_i32_e64 s[16:17], v44, v78
	v_mad_u32_u24 v44, v44, s36, v240
	v_add3_u32 v108, s92, v56, v51
	v_cmp_gt_i32_e64 s[22:23], v79, v57
	v_cmp_gt_i32_e64 s[24:25], v79, v68
	v_cmp_lt_i32_e64 s[26:27], v79, v68
	v_mul_u32_u24_e32 v51, 0x48, v43
	v_mad_u32_u24 v57, v43, s36, v240
	v_mad_u32_u24 v68, v43, s36, v241
	v_mad_u32_u24 v43, v43, s36, v242
	s_movk_i32 s0, 0x88
	v_add_lshl_u32 v47, v47, v48, 1
	v_add_lshl_u32 v54, v45, v48, 1
	v_add_lshl_u32 v49, v49, v48, 1
	v_add_lshl_u32 v80, v44, v48, 1
	v_add_lshl_u32 v112, v48, v51, 1
	v_add_lshl_u32 v113, v57, v48, 1
	v_add_lshl_u32 v114, v68, v48, 1
	v_add_lshl_u32 v115, v43, v48, 1
	v_add_lshl_u32 v48, v50, v43, 1
	v_mul_lo_u32 v43, v106, s0
	s_sub_i32 s56, 0, s45
	v_readfirstlane_b32 s0, v34
	s_mul_i32 s1, s56, s0
	s_mul_hi_u32 s1, s0, s1
	s_add_i32 s57, s0, s1
	s_lshl_b32 s0, s49, 8
	s_add_u32 s0, s40, s0
	v_cmp_gt_i32_e64 s[28:29], v79, v78
	v_cmp_lt_i32_e64 s[30:31], v79, v78
	v_add_lshl_u32 v78, v50, v68, 1
	s_addc_u32 s1, s41, 0
	v_lshlrev_b32_e32 v68, 1, v92
	v_lshlrev_b32_e32 v36, 3, v38
	v_lshlrev_b32_e32 v38, 4, v38
	v_add_u32_e32 v52, 0, v42
	v_add_lshl_u32 v45, v45, v50, 1
	v_add_lshl_u32 v44, v44, v50, 1
	v_add_lshl_u32 v51, v50, v51, 1
	v_add_lshl_u32 v57, v50, v57, 1
	v_mul_u32_u24_e32 v46, 0x440, v46
	v_add_lshl_u32 v117, v43, v92, 1
	v_lshl_add_u64 v[98:99], s[0:1], 0, v[68:69]
	v_mov_b32_e32 v43, v69
	s_lshl_b32 s0, s45, 12
	v_add_u32_e32 v107, 32, v106
	v_lshl_add_u64 v[100:101], v[40:41], 0, v[42:43]
	s_lshl_b32 s36, s45, 6
	s_sub_i32 s37, 0, s0
	s_add_i32 s0, s84, s44
	v_add_u32_e32 v120, v37, v39
	v_lshlrev_b32_e32 v68, 1, v36
	v_lshlrev_b32_e32 v102, 1, v38
	v_add_u32_e32 v121, 0, v47
	v_add_u32_e32 v122, 0, v54
	v_add_u32_e32 v123, 0, v49
	v_add_u32_e32 v124, 0, v45
	v_add_u32_e32 v125, v55, v56
	v_add_u32_e32 v127, 0, v44
	v_add_u32_e32 v128, v52, v35
	v_and_b32_e32 v190, 7, v0
	v_lshrrev_b32_e32 v191, 6, v0
	v_mul_u32_u24_e32 v120, 0x900, v190
	v_lshl_add_u32 v120, v191, 4, v120
	v_bfe_u32 v192, v0, 3, 3
	v_and_b32_e32 v193, 1, v192
	v_mul_u32_u24_e32 v194, 0x90, v193
	v_add_u32_e32 v120, v120, v194
	v_and_b32_e32 v192, 6, v192
	v_lshl_add_u32 v120, v192, 1, v120
	v_mov_b32_e32 v191, 0x5040100
	v_mov_b32_e32 v194, 0x3020706
	v_cmp_eq_u32_e32 vcc, 1, v193
	s_nop 1
	v_cndmask_b32_e32 v191, v191, v194, vcc
	v_add_u32_e32 v129, 0, v51
	v_add_u32_e32 v130, 0, v57
	v_add_u32_e32 v132, 0, v48
	v_add_u32_e32 v133, v53, v46
	s_waitcnt vmcnt(2)
	v_mov_b64_e32 v[54:55], v[62:63]
	v_mov_b64_e32 v[46:47], v[74:75]
	v_mov_b64_e32 v[50:51], v[58:59]
	v_mov_b64_e32 v[38:39], v[70:71]
	v_mov_b64_e32 v[44:45], v[20:21]
	v_mov_b64_e32 v[36:37], v[24:25]
	s_mov_b32 s97, s67
	v_mov_b32_e32 v93, v69
	v_add_u32_e32 v109, 0x90, v108
	v_add_u32_e32 v110, 0x120, v108
	v_add_u32_e32 v111, 0x1b0, v108
	v_lshl_add_u32 v116, v106, 2, s35
	v_lshl_add_u32 v118, v107, 2, s35
	v_add_u32_e32 v119, 0x2200, v117
	s_lshl_b32 s71, s44, 6
	s_lshl_b32 s74, s84, 6
	s_sub_i32 s75, 0, s36
	s_lshl_b32 s79, s44, 12
	s_lshl_b32 s80, s84, 12
	s_sub_i32 s81, 0xffffffc0, s0
	s_lshl_b32 s66, s34, 1
	v_add_u32_e32 v126, 0, v80
	v_add_u32_e32 v131, 0, v78
	v_mov_b64_e32 v[56:57], v[64:65]
	v_mov_b64_e32 v[48:49], v[76:77]
	v_mov_b64_e32 v[52:53], v[60:61]
	v_mov_b64_e32 v[40:41], v[72:73]
	v_mov_b64_e32 v[42:43], v[18:19]
	v_mov_b64_e32 v[34:35], v[22:23]
	s_branch .LBB0_661

.LBB0_661:
	s_add_i32 s0, 0, 0x1b000
	v_add_u32_e32 v78, s0, v90
	v_readlane_b32 s34, v247, 23
	ds_write_b128 v78, v[14:17]
	v_mov_b32_e32 v86, v69
	v_add_u32_e32 v78, s34, v90
	ds_write_b128 v78, v[10:13]
	v_mov_b32_dpp v192, v2 row_ror:8 row_mask:0xf bank_mask:0xf
	v_mov_b32_dpp v193, v3 row_ror:8 row_mask:0xf bank_mask:0xf
	v_mov_b32_dpp v194, v4 row_ror:8 row_mask:0xf bank_mask:0xf
	v_mov_b32_dpp v195, v5 row_ror:8 row_mask:0xf bank_mask:0xf
	v_perm_b32 v192, v192, v2, v191
	v_perm_b32 v193, v193, v3, v191
	v_perm_b32 v194, v194, v4, v191
	v_perm_b32 v195, v195, v5, v191
	ds_write_b32 v120, v192 offset:54272
	ds_write_b32 v120, v193 offset:54560
	ds_write_b32 v120, v194 offset:54848
	ds_write_b32 v120, v195 offset:55136
	v_mov_b32_dpp v192, v6 row_ror:8 row_mask:0xf bank_mask:0xf
	v_mov_b32_dpp v193, v7 row_ror:8 row_mask:0xf bank_mask:0xf
	v_mov_b32_dpp v194, v8 row_ror:8 row_mask:0xf bank_mask:0xf
	v_mov_b32_dpp v195, v9 row_ror:8 row_mask:0xf bank_mask:0xf
	v_perm_b32 v192, v192, v6, v191
	v_perm_b32 v193, v193, v7, v191
	v_perm_b32 v194, v194, v8, v191
	v_perm_b32 v195, v195, v9, v191
	ds_write_b32 v120, v192 offset:55424
	ds_write_b32 v120, v193 offset:55712
	ds_write_b32 v120, v194 offset:56000
	ds_write_b32 v120, v195 offset:56288
	s_waitcnt vmcnt(1)
	v_lshlrev_b32_e32 v78, 16, v26
	v_and_b32_e32 v79, 0xffff0000, v26
	v_lshlrev_b32_e32 v80, 16, v27
	v_add_f32_dpp v78, v78, v78 row_shr:1 row_mask:0xf bank_mask:0xf bound_ctrl:1
	v_and_b32_e32 v81, 0xffff0000, v27
	v_lshlrev_b32_e32 v82, 16, v28
	v_add_f32_dpp v78, v78, v78 row_shr:2 row_mask:0xf bank_mask:0xf bound_ctrl:1
	v_and_b32_e32 v83, 0xffff0000, v28
	v_lshlrev_b32_e32 v84, 16, v29
	v_add_f32_dpp v78, v78, v78 row_shr:4 row_mask:0xf bank_mask:0xf bound_ctrl:1
	v_and_b32_e32 v85, 0xffff0000, v29
	v_mov_b32_e32 v87, v69
	v_add_f32_dpp v78, v78, v78 row_shr:8 row_mask:0xf bank_mask:0xf bound_ctrl:1
	s_waitcnt lgkmcnt(0)
	s_barrier
	s_add_i32 s65, s44, s84
	v_mov_b32_dpp v86, v78 row_bcast:15 row_mask:0xa bank_mask:0xf bound_ctrl:1
	v_add_f32_e32 v78, v78, v86
	v_mov_b32_e32 v86, v69
	s_add_i32 s85, s84, 64
	s_cmp_ge_i32 s85, s48
	v_mov_b32_dpp v86, v78 row_bcast:31 row_mask:0xc bank_mask:0xf bound_ctrl:1
	v_add_f32_e32 v103, v78, v86
	v_add_f32_dpp v78, v79, v79 row_shr:1 row_mask:0xf bank_mask:0xf bound_ctrl:1
	v_mov_b32_e32 v79, v69
	s_cselect_b64 s[86:87], -1, 0
	v_add_f32_dpp v78, v78, v78 row_shr:2 row_mask:0xf bank_mask:0xf bound_ctrl:1
	s_and_b64 vcc, exec, s[86:87]
	s_nop 0
	v_add_f32_dpp v78, v78, v78 row_shr:4 row_mask:0xf bank_mask:0xf bound_ctrl:1
	s_nop 1
	v_add_f32_dpp v78, v78, v78 row_shr:8 row_mask:0xf bank_mask:0xf bound_ctrl:1
	s_nop 1
	v_mov_b32_dpp v79, v78 row_bcast:15 row_mask:0xa bank_mask:0xf bound_ctrl:1
	v_add_f32_e32 v78, v78, v79
	v_mov_b32_e32 v79, v69
	s_nop 1
	v_mov_b32_dpp v79, v78 row_bcast:31 row_mask:0xc bank_mask:0xf bound_ctrl:1
	v_add_f32_e32 v146, v78, v79
	v_add_f32_dpp v78, v80, v80 row_shr:1 row_mask:0xf bank_mask:0xf bound_ctrl:1
	v_mov_b32_e32 v79, v69
	s_waitcnt vmcnt(0)
	v_lshlrev_b32_e32 v80, 16, v31
	v_add_f32_dpp v78, v78, v78 row_shr:2 row_mask:0xf bank_mask:0xf bound_ctrl:1
	s_nop 1
	v_add_f32_dpp v78, v78, v78 row_shr:4 row_mask:0xf bank_mask:0xf bound_ctrl:1
	s_nop 1
	v_add_f32_dpp v78, v78, v78 row_shr:8 row_mask:0xf bank_mask:0xf bound_ctrl:1
	s_nop 1
	v_mov_b32_dpp v79, v78 row_bcast:15 row_mask:0xa bank_mask:0xf bound_ctrl:1
	v_add_f32_e32 v78, v78, v79
	v_mov_b32_e32 v79, v69
	s_nop 1
	v_mov_b32_dpp v79, v78 row_bcast:31 row_mask:0xc bank_mask:0xf bound_ctrl:1
	v_add_f32_e32 v147, v78, v79
	v_add_f32_dpp v78, v81, v81 row_shr:1 row_mask:0xf bank_mask:0xf bound_ctrl:1
	v_mov_b32_e32 v79, v69
	v_and_b32_e32 v81, 0xffff0000, v31
	v_add_f32_dpp v78, v78, v78 row_shr:2 row_mask:0xf bank_mask:0xf bound_ctrl:1
	s_nop 1
	v_add_f32_dpp v78, v78, v78 row_shr:4 row_mask:0xf bank_mask:0xf bound_ctrl:1
	s_nop 1
	v_add_f32_dpp v78, v78, v78 row_shr:8 row_mask:0xf bank_mask:0xf bound_ctrl:1
	s_nop 1
	v_mov_b32_dpp v79, v78 row_bcast:15 row_mask:0xa bank_mask:0xf bound_ctrl:1
	v_add_f32_e32 v78, v78, v79
	v_mov_b32_e32 v79, v69
	s_nop 1
	v_mov_b32_dpp v79, v78 row_bcast:31 row_mask:0xc bank_mask:0xf bound_ctrl:1
	v_add_f32_e32 v148, v78, v79
	v_add_f32_dpp v78, v82, v82 row_shr:1 row_mask:0xf bank_mask:0xf bound_ctrl:1
	v_mov_b32_e32 v79, v69
	v_lshlrev_b32_e32 v82, 16, v32
	v_add_f32_dpp v78, v78, v78 row_shr:2 row_mask:0xf bank_mask:0xf bound_ctrl:1
	s_nop 1
	v_add_f32_dpp v78, v78, v78 row_shr:4 row_mask:0xf bank_mask:0xf bound_ctrl:1
	s_nop 1
	v_add_f32_dpp v78, v78, v78 row_shr:8 row_mask:0xf bank_mask:0xf bound_ctrl:1
	s_nop 1
	v_mov_b32_dpp v79, v78 row_bcast:15 row_mask:0xa bank_mask:0xf bound_ctrl:1
	v_add_f32_e32 v78, v78, v79
	v_mov_b32_e32 v79, v69
	s_nop 1
	v_mov_b32_dpp v79, v78 row_bcast:31 row_mask:0xc bank_mask:0xf bound_ctrl:1
	v_add_f32_e32 v149, v78, v79
	v_add_f32_dpp v78, v83, v83 row_shr:1 row_mask:0xf bank_mask:0xf bound_ctrl:1
	v_mov_b32_e32 v79, v69
	v_and_b32_e32 v83, 0xffff0000, v32
	v_add_f32_dpp v78, v78, v78 row_shr:2 row_mask:0xf bank_mask:0xf bound_ctrl:1
	s_nop 1
	v_add_f32_dpp v78, v78, v78 row_shr:4 row_mask:0xf bank_mask:0xf bound_ctrl:1
	s_nop 1
	v_add_f32_dpp v78, v78, v78 row_shr:8 row_mask:0xf bank_mask:0xf bound_ctrl:1
	s_nop 1
	v_mov_b32_dpp v79, v78 row_bcast:15 row_mask:0xa bank_mask:0xf bound_ctrl:1
	v_add_f32_e32 v78, v78, v79
	v_mov_b32_e32 v79, v69
	s_nop 1
	v_mov_b32_dpp v79, v78 row_bcast:31 row_mask:0xc bank_mask:0xf bound_ctrl:1
	v_add_f32_e32 v150, v78, v79
	v_add_f32_dpp v78, v84, v84 row_shr:1 row_mask:0xf bank_mask:0xf bound_ctrl:1
	v_mov_b32_e32 v79, v69
	v_lshlrev_b32_e32 v84, 16, v33
	v_add_f32_dpp v78, v78, v78 row_shr:2 row_mask:0xf bank_mask:0xf bound_ctrl:1
	s_nop 1
	v_add_f32_dpp v78, v78, v78 row_shr:4 row_mask:0xf bank_mask:0xf bound_ctrl:1
	s_nop 1
	v_add_f32_dpp v78, v78, v78 row_shr:8 row_mask:0xf bank_mask:0xf bound_ctrl:1
	s_nop 1
	v_mov_b32_dpp v79, v78 row_bcast:15 row_mask:0xa bank_mask:0xf bound_ctrl:1
	v_add_f32_e32 v78, v78, v79
	v_mov_b32_e32 v79, v69
	s_nop 1
	v_mov_b32_dpp v79, v78 row_bcast:31 row_mask:0xc bank_mask:0xf bound_ctrl:1
	v_add_f32_e32 v151, v78, v79
	v_add_f32_dpp v78, v85, v85 row_shr:1 row_mask:0xf bank_mask:0xf bound_ctrl:1
	v_mov_b32_e32 v79, v69
	v_and_b32_e32 v85, 0xffff0000, v33
	v_add_f32_dpp v78, v78, v78 row_shr:2 row_mask:0xf bank_mask:0xf bound_ctrl:1
	s_nop 1
	v_add_f32_dpp v78, v78, v78 row_shr:4 row_mask:0xf bank_mask:0xf bound_ctrl:1
	s_nop 1
	v_add_f32_dpp v78, v78, v78 row_shr:8 row_mask:0xf bank_mask:0xf bound_ctrl:1
	s_nop 1
	v_mov_b32_dpp v79, v78 row_bcast:15 row_mask:0xa bank_mask:0xf bound_ctrl:1
	v_add_f32_e32 v78, v78, v79
	v_mov_b32_e32 v79, v69
	s_nop 1
	v_mov_b32_dpp v79, v78 row_bcast:31 row_mask:0xc bank_mask:0xf bound_ctrl:1
	v_add_f32_e32 v152, v78, v79
	v_lshlrev_b32_e32 v78, 16, v30
	v_and_b32_e32 v79, 0xffff0000, v30
	s_nop 0
	v_add_f32_dpp v86, v78, v78 row_shr:1 row_mask:0xf bank_mask:0xf bound_ctrl:1
	s_nop 1
	v_add_f32_dpp v86, v86, v86 row_shr:2 row_mask:0xf bank_mask:0xf bound_ctrl:1
	s_nop 1
	v_add_f32_dpp v86, v86, v86 row_shr:4 row_mask:0xf bank_mask:0xf bound_ctrl:1
	s_nop 1
	v_add_f32_dpp v86, v86, v86 row_shr:8 row_mask:0xf bank_mask:0xf bound_ctrl:1
	s_nop 1
	v_mov_b32_dpp v87, v86 row_bcast:15 row_mask:0xa bank_mask:0xf bound_ctrl:1
	v_add_f32_e32 v86, v86, v87
	v_mov_b32_e32 v87, v69
	s_nop 1
	v_mov_b32_dpp v87, v86 row_bcast:31 row_mask:0xc bank_mask:0xf bound_ctrl:1
	v_add_f32_e32 v86, v86, v87
	v_mul_f32_e32 v87, 0x3fb8aa3b, v146
	v_readlane_b32 s1, v86, 63
	v_exp_f32_e32 v87, v87
	s_nop 0
	v_sub_f32_e32 v86, s1, v86
	v_add_f32_e32 v153, v86, v78
	v_add_f32_dpp v78, v79, v79 row_shr:1 row_mask:0xf bank_mask:0xf bound_ctrl:1
	v_mov_b32_e32 v86, v69
	s_nop 0
	v_add_f32_dpp v78, v78, v78 row_shr:2 row_mask:0xf bank_mask:0xf bound_ctrl:1
	s_nop 1
	v_add_f32_dpp v78, v78, v78 row_shr:4 row_mask:0xf bank_mask:0xf bound_ctrl:1
	s_nop 1
	v_add_f32_dpp v78, v78, v78 row_shr:8 row_mask:0xf bank_mask:0xf bound_ctrl:1
	s_nop 1
	v_mov_b32_dpp v86, v78 row_bcast:15 row_mask:0xa bank_mask:0xf bound_ctrl:1
	v_add_f32_e32 v78, v78, v86
	v_mov_b32_e32 v86, v69
	s_nop 1
	v_mov_b32_dpp v86, v78 row_bcast:31 row_mask:0xc bank_mask:0xf bound_ctrl:1
	v_add_f32_e32 v78, v78, v86
	v_mul_f32_e32 v86, 0x3fb8aa3b, v103
	v_readlane_b32 s1, v78, 63
	v_exp_f32_e32 v86, v86
	s_nop 0
	v_sub_f32_e32 v78, s1, v78
	v_add_f32_e32 v154, v78, v79
	v_mov_b32_e32 v79, v69
	v_add_f32_dpp v78, v80, v80 row_shr:1 row_mask:0xf bank_mask:0xf bound_ctrl:1
	s_nop 1
	v_add_f32_dpp v78, v78, v78 row_shr:2 row_mask:0xf bank_mask:0xf bound_ctrl:1
	s_nop 1
	v_add_f32_dpp v78, v78, v78 row_shr:4 row_mask:0xf bank_mask:0xf bound_ctrl:1
	s_nop 1
	v_add_f32_dpp v78, v78, v78 row_shr:8 row_mask:0xf bank_mask:0xf bound_ctrl:1
	s_nop 1
	v_mov_b32_dpp v79, v78 row_bcast:15 row_mask:0xa bank_mask:0xf bound_ctrl:1
	v_add_f32_e32 v78, v78, v79
	v_mov_b32_e32 v79, v69
	s_nop 1
	v_mov_b32_dpp v79, v78 row_bcast:31 row_mask:0xc bank_mask:0xf bound_ctrl:1
	v_add_f32_e32 v78, v78, v79
	v_mov_b32_e32 v79, v69
	v_readlane_b32 s1, v78, 63
	s_nop 1
	v_sub_f32_e32 v78, s1, v78
	v_add_f32_e32 v155, v78, v80
	s_nop 0
	v_add_f32_dpp v78, v81, v81 row_shr:1 row_mask:0xf bank_mask:0xf bound_ctrl:1
	s_nop 1
	v_add_f32_dpp v78, v78, v78 row_shr:2 row_mask:0xf bank_mask:0xf bound_ctrl:1
	s_nop 1
	v_add_f32_dpp v78, v78, v78 row_shr:4 row_mask:0xf bank_mask:0xf bound_ctrl:1
	s_nop 1
	v_add_f32_dpp v78, v78, v78 row_shr:8 row_mask:0xf bank_mask:0xf bound_ctrl:1
	s_nop 1
	v_mov_b32_dpp v79, v78 row_bcast:15 row_mask:0xa bank_mask:0xf bound_ctrl:1
	v_add_f32_e32 v78, v78, v79
	v_mov_b32_e32 v79, v69
	s_nop 1
	v_mov_b32_dpp v79, v78 row_bcast:31 row_mask:0xc bank_mask:0xf bound_ctrl:1
	v_add_f32_e32 v78, v78, v79
	v_mov_b32_e32 v79, v69
	v_readlane_b32 s1, v78, 63
	s_nop 1
	v_sub_f32_e32 v78, s1, v78
	v_add_f32_e32 v156, v78, v81
	s_nop 0
	v_add_f32_dpp v78, v82, v82 row_shr:1 row_mask:0xf bank_mask:0xf bound_ctrl:1
	s_nop 1
	v_add_f32_dpp v78, v78, v78 row_shr:2 row_mask:0xf bank_mask:0xf bound_ctrl:1
	s_nop 1
	v_add_f32_dpp v78, v78, v78 row_shr:4 row_mask:0xf bank_mask:0xf bound_ctrl:1
	s_nop 1
	v_add_f32_dpp v78, v78, v78 row_shr:8 row_mask:0xf bank_mask:0xf bound_ctrl:1
	s_nop 1
	v_mov_b32_dpp v79, v78 row_bcast:15 row_mask:0xa bank_mask:0xf bound_ctrl:1
	v_add_f32_e32 v78, v78, v79
	v_mov_b32_e32 v79, v69
	s_nop 1
	v_mov_b32_dpp v79, v78 row_bcast:31 row_mask:0xc bank_mask:0xf bound_ctrl:1
	v_add_f32_e32 v78, v78, v79
	v_mov_b32_e32 v79, v69
	v_readlane_b32 s1, v78, 63
	s_nop 1
	v_sub_f32_e32 v78, s1, v78
	v_add_f32_e32 v157, v78, v82
	v_add_u32_e32 v82, s0, v105
	v_add_f32_dpp v78, v83, v83 row_shr:1 row_mask:0xf bank_mask:0xf bound_ctrl:1
	s_mov_b32 s0, 0x3e000000
	s_nop 0
	v_add_f32_dpp v78, v78, v78 row_shr:2 row_mask:0xf bank_mask:0xf bound_ctrl:1
	s_nop 1
	v_add_f32_dpp v78, v78, v78 row_shr:4 row_mask:0xf bank_mask:0xf bound_ctrl:1
	s_nop 1
	v_add_f32_dpp v78, v78, v78 row_shr:8 row_mask:0xf bank_mask:0xf bound_ctrl:1
	s_nop 1
	v_mov_b32_dpp v79, v78 row_bcast:15 row_mask:0xa bank_mask:0xf bound_ctrl:1
	v_add_f32_e32 v78, v78, v79
	v_mov_b32_e32 v79, v69
	s_nop 1
	v_mov_b32_dpp v79, v78 row_bcast:31 row_mask:0xc bank_mask:0xf bound_ctrl:1
	v_add_f32_e32 v78, v78, v79
	v_mov_b32_e32 v79, v69
	v_readlane_b32 s1, v78, 63
	s_nop 1
	v_sub_f32_e32 v78, s1, v78
	v_add_f32_e32 v158, v78, v83
	s_nop 0
	v_add_f32_dpp v78, v84, v84 row_shr:1 row_mask:0xf bank_mask:0xf bound_ctrl:1
	s_nop 1
	v_add_f32_dpp v78, v78, v78 row_shr:2 row_mask:0xf bank_mask:0xf bound_ctrl:1
	s_nop 1
	v_add_f32_dpp v78, v78, v78 row_shr:4 row_mask:0xf bank_mask:0xf bound_ctrl:1
	s_nop 1
	v_add_f32_dpp v78, v78, v78 row_shr:8 row_mask:0xf bank_mask:0xf bound_ctrl:1
	s_nop 1
	v_mov_b32_dpp v79, v78 row_bcast:15 row_mask:0xa bank_mask:0xf bound_ctrl:1
	v_add_f32_e32 v78, v78, v79
	v_mov_b32_e32 v79, v69
	s_nop 1
	v_mov_b32_dpp v79, v78 row_bcast:31 row_mask:0xc bank_mask:0xf bound_ctrl:1
	v_add_f32_e32 v78, v78, v79
	v_mov_b32_e32 v79, v69
	v_readlane_b32 s1, v78, 63
	s_nop 1
	v_sub_f32_e32 v78, s1, v78
	v_add_f32_e32 v159, v78, v84
	s_nop 0
	v_add_f32_dpp v78, v85, v85 row_shr:1 row_mask:0xf bank_mask:0xf bound_ctrl:1
	s_nop 1
	v_add_f32_dpp v78, v78, v78 row_shr:2 row_mask:0xf bank_mask:0xf bound_ctrl:1
	s_nop 1
	v_add_f32_dpp v78, v78, v78 row_shr:4 row_mask:0xf bank_mask:0xf bound_ctrl:1
	s_nop 1
	v_add_f32_dpp v78, v78, v78 row_shr:8 row_mask:0xf bank_mask:0xf bound_ctrl:1
	s_nop 1
	v_mov_b32_dpp v79, v78 row_bcast:15 row_mask:0xa bank_mask:0xf bound_ctrl:1
	v_add_f32_e32 v78, v78, v79
	v_mov_b32_e32 v79, v69
	s_nop 1
	v_mov_b32_dpp v79, v78 row_bcast:31 row_mask:0xc bank_mask:0xf bound_ctrl:1
	v_add_f32_e32 v78, v78, v79
	s_nop 0
	v_readlane_b32 s1, v78, 63
	s_nop 1
	v_sub_f32_e32 v78, s1, v78
	v_add_f32_e32 v160, v78, v85
	v_add_u32_e32 v78, s34, v105
	ds_read_b128 v[78:81], v78
	ds_read_b128 v[82:85], v82
	s_waitcnt lgkmcnt(1)
	v_lshlrev_b32_e32 v88, 16, v78
	v_and_b32_e32 v89, 0xffff0000, v78
	v_mul_f32_e32 v78, 0x3fb8aa3b, v147
	v_exp_f32_e32 v134, v78
	v_mul_f32_e32 v78, 0x3fb8aa3b, v148
	v_exp_f32_e32 v135, v78
	v_lshlrev_b32_e32 v78, 16, v79
	v_and_b32_e32 v79, 0xffff0000, v79
	v_pk_mul_f32 v[136:137], v[78:79], s[0:1] op_sel_hi:[1,0]
	v_mul_f32_e32 v78, 0x3fb8aa3b, v149
	v_mul_f32_e32 v79, 0x3fb8aa3b, v150
	v_exp_f32_e32 v78, v78
	v_exp_f32_e32 v79, v79
	v_lshlrev_b32_e32 v138, 16, v80
	v_and_b32_e32 v139, 0xffff0000, v80
	v_pk_mul_f32 v[138:139], v[138:139], s[0:1] op_sel_hi:[1,0]
	v_lshlrev_b32_e32 v80, 16, v81
	v_pk_mul_f32 v[140:141], v[78:79], v[138:139]
	v_mul_f32_e32 v78, 0x3fb8aa3b, v151
	v_mul_f32_e32 v79, 0x3fb8aa3b, v152
	v_exp_f32_e32 v78, v78
	v_exp_f32_e32 v79, v79
	v_and_b32_e32 v81, 0xffff0000, v81
	v_pk_mul_f32 v[88:89], v[88:89], s[0:1] op_sel_hi:[1,0]
	v_pk_mul_f32 v[142:143], v[80:81], s[0:1] op_sel_hi:[1,0]
	v_pk_mul_f32 v[86:87], v[86:87], v[88:89]
	v_pk_mul_f32 v[134:135], v[134:135], v[136:137]
	v_pk_mul_f32 v[144:145], v[78:79], v[142:143]
	v_cvt_pk_bf16_f32 v78, v86, v87
	v_cvt_pk_bf16_f32 v79, v134, v135
	v_cvt_pk_bf16_f32 v80, v140, v141
	v_cvt_pk_bf16_f32 v81, v144, v145
	v_add_u32_e32 v140, 0, v105
	ds_write_b128 v140, v[78:81] offset:35840
	v_mul_f32_e32 v78, 0x3fb8aa3b, v153
	v_mul_f32_e32 v79, 0x3fb8aa3b, v154
	v_exp_f32_e32 v78, v78
	v_exp_f32_e32 v79, v79
	v_mul_f32_e32 v80, 0x3fb8aa3b, v155
	v_mul_f32_e32 v81, 0x3fb8aa3b, v156
	v_mul_f32_e32 v86, 0x3fb8aa3b, v157
	v_pk_mul_f32 v[78:79], v[78:79], v[88:89]
	v_mul_f32_e32 v87, 0x3fb8aa3b, v158
	v_mul_f32_e32 v88, 0x3fb8aa3b, v159
	v_mul_f32_e32 v89, 0x3fb8aa3b, v160
	v_exp_f32_e32 v80, v80
	v_exp_f32_e32 v81, v81
	v_exp_f32_e32 v86, v86
	v_exp_f32_e32 v87, v87
	v_exp_f32_e32 v88, v88
	v_exp_f32_e32 v89, v89
	v_pk_mul_f32 v[80:81], v[80:81], v[136:137]
	v_pk_mul_f32 v[86:87], v[86:87], v[138:139]
	v_cvt_pk_bf16_f32 v78, v78, v79
	v_pk_mul_f32 v[88:89], v[88:89], v[142:143]
	v_cvt_pk_bf16_f32 v79, v80, v81
	v_cvt_pk_bf16_f32 v80, v86, v87
	v_cvt_pk_bf16_f32 v81, v88, v89
	s_waitcnt lgkmcnt(1)
	v_lshlrev_b32_e32 v134, 16, v84
	v_and_b32_e32 v135, 0xffff0000, v84
	v_mul_f32_e32 v84, 0xbfb8aa3b, v151
	ds_write_b128 v140, v[78:81] offset:45056
	v_mul_f32_e32 v78, 0xbfb8aa3b, v103
	v_mul_f32_e32 v79, 0xbfb8aa3b, v146
	v_mul_f32_e32 v80, 0xbfb8aa3b, v147
	v_mul_f32_e32 v81, 0xbfb8aa3b, v148
	v_mul_f32_e32 v88, 0xbfb8aa3b, v149
	v_mul_f32_e32 v89, 0xbfb8aa3b, v150
	v_exp_f32_e32 v136, v84
	v_mul_f32_e32 v84, 0xbfb8aa3b, v152
	v_exp_f32_e32 v78, v78
	v_exp_f32_e32 v79, v79
	v_exp_f32_e32 v80, v80
	v_exp_f32_e32 v81, v81
	v_exp_f32_e32 v88, v88
	v_exp_f32_e32 v89, v89
	v_exp_f32_e32 v137, v84
	v_lshlrev_b32_e32 v86, 16, v82
	v_and_b32_e32 v87, 0xffff0000, v82
	v_lshlrev_b32_e32 v82, 16, v83
	v_and_b32_e32 v83, 0xffff0000, v83
	v_lshlrev_b32_e32 v84, 16, v85
	v_and_b32_e32 v85, 0xffff0000, v85
	v_pk_mul_f32 v[78:79], v[78:79], v[86:87]
	v_pk_mul_f32 v[80:81], v[80:81], v[82:83]
	v_pk_mul_f32 v[88:89], v[88:89], v[134:135]
	v_pk_mul_f32 v[136:137], v[136:137], v[84:85]
	v_cvt_pk_bf16_f32 v78, v78, v79
	v_cvt_pk_bf16_f32 v79, v80, v81
	v_cvt_pk_bf16_f32 v80, v88, v89
	v_cvt_pk_bf16_f32 v81, v136, v137
	ds_write_b128 v140, v[78:81] offset:17408
	v_mul_f32_e32 v78, 0xbfb8aa3b, v153
	v_mul_f32_e32 v79, 0xbfb8aa3b, v154
	v_mul_f32_e32 v80, 0xbfb8aa3b, v155
	v_mul_f32_e32 v81, 0xbfb8aa3b, v156
	v_exp_f32_e32 v78, v78
	v_exp_f32_e32 v79, v79
	v_exp_f32_e32 v80, v80
	v_exp_f32_e32 v81, v81
	v_pk_mul_f32 v[78:79], v[78:79], v[86:87]
	v_mul_f32_e32 v86, 0xbfb8aa3b, v159
	v_pk_mul_f32 v[80:81], v[80:81], v[82:83]
	v_mul_f32_e32 v82, 0xbfb8aa3b, v157
	v_mul_f32_e32 v83, 0xbfb8aa3b, v158
	v_mul_f32_e32 v87, 0xbfb8aa3b, v160
	v_exp_f32_e32 v82, v82
	v_exp_f32_e32 v83, v83
	v_exp_f32_e32 v86, v86
	v_exp_f32_e32 v87, v87
	v_cvt_pk_bf16_f32 v78, v78, v79
	v_pk_mul_f32 v[82:83], v[82:83], v[134:135]
	v_cvt_pk_bf16_f32 v79, v80, v81
	v_pk_mul_f32 v[84:85], v[86:87], v[84:85]
	v_cvt_pk_bf16_f32 v80, v82, v83
	v_cvt_pk_bf16_f32 v81, v84, v85
	ds_write_b128 v140, v[78:81] offset:26624
	s_cbranch_vccnz .LBB0_676
	s_ashr_i32 s89, s85, 31
	s_add_i32 s0, s84, s89
	s_add_i32 s0, s0, 64
	s_xor_b32 s0, s0, s89
	s_mul_hi_u32 s1, s0, s57
	s_mul_i32 s34, s1, s45
	s_sub_i32 s0, s0, s34
	s_add_i32 s34, s1, 1
	s_sub_i32 s35, s0, s45
	s_cmp_ge_u32 s0, s45
	s_cselect_b32 s1, s34, s1
	s_cselect_b32 s0, s35, s0
	s_add_i32 s34, s1, 1
	s_cmp_ge_u32 s0, s45
	s_cselect_b32 s0, s34, s1
	s_xor_b32 s90, s0, s89
	s_sub_i32 s88, s90, s89
	s_mul_i32 s0, s56, s88
	s_add_i32 s91, s65, s0
	s_add_i32 s69, s91, 64
	s_cmp_lt_i32 s69, 4
	s_mov_b64 s[34:35], -1
	s_cselect_b64 s[0:1], -1, 0
	s_cmp_gt_i32 s69, 3
	s_mul_i32 s70, s36, s88
	s_cbranch_scc1 .LBB0_664
	s_lshl_b32 s34, s90, 8
	s_sub_i32 s34, s34, s70
	s_lshl_b32 s35, s89, 8
	s_sub_i32 s34, s34, s35
	s_add_i32 s35, s71, s74
	s_add_i32 s34, s35, s34
	s_add_i32 s77, s34, 0x1000
	s_mov_b64 s[34:35], 0
